# NA attention loop: bias loads of tile t+1 prefetched one iteration ahead into own registers; V(t) waited only before PV MFMAs
# speedup vs baseline: 1.0062x; 1.0062x over previous
.LBB0_1292:
	s_ashr_i32 s47, s33, 4
	v_bfrev_b32_e32 v0, 0.5
	v_med3_i32 v4, s47, 4, v0
	s_lshl_b32 s1, s33, 5
	v_readfirstlane_b32 s0, v4
	s_add_i32 s48, s0, -4
	s_lshl_b32 s0, s47, 6
	s_and_b32 s46, s1, 32
	s_or_b32 s2, s0, s46
	s_bfe_u32 s9, s33, 0x30001
	s_ashr_i32 s3, s2, 31
	s_lshl_b32 s80, s9, 22
	s_lshl_b64 s[0:1], s[2:3], 11
	s_add_u32 s0, s20, s0
	s_addc_u32 s1, s21, s1
	s_lshl_b32 s34, s9, 7
	s_lshl_b32 s3, s9, 8
	s_add_u32 s0, s0, s3
	s_addc_u32 s1, s1, 0
	s_lshl_b32 s3, s9, 21
	s_add_u32 s49, s22, s80
	v_readlane_b32 s35, v255, 17
	s_addc_u32 s50, s23, 0
	s_or_b32 s9, s9, s35
	s_mul_i32 s36, s9, 0x780
	s_mov_b32 s37, s81
	s_lshl_b32 s8, s48, 1
	s_lshl_b64 s[36:37], s[36:37], 2
	s_add_u32 s35, s30, s36
	s_mov_b32 s9, s81
	s_addc_u32 s36, s31, s37
	v_lshl_add_u64 v[0:1], s[0:1], 0, v[176:177]
	v_lshlrev_b32_e32 v2, 1, v172
	v_mov_b32_e32 v3, v177
	s_lshl_b64 s[0:1], s[8:9], 12
	s_lshl_b64 s[8:9], s[8:9], 13
	v_lshl_add_u64 v[0:1], v[0:1], 0, v[2:3]
	v_or_b32_e32 v2, s46, v173
	s_add_u32 s8, s49, s8
	global_load_dwordx4 v[108:111], v[0:1], off
	global_load_dwordx4 v[104:107], v[0:1], off offset:32
	global_load_dwordx4 v[100:103], v[0:1], off offset:64
	global_load_dwordx4 v[96:99], v[0:1], off offset:96
	global_load_dwordx4 v[92:95], v[0:1], off offset:128
	global_load_dwordx4 v[88:91], v[0:1], off offset:160
	global_load_dwordx4 v[84:87], v[0:1], off offset:192
	global_load_dwordx4 v[80:83], v[0:1], off offset:224
	v_min_u32_e32 v0, 56, v2
	s_addc_u32 s9, s50, s9
	v_mov_b32_e32 v199, v177
	v_sub_u32_e32 v3, 8, v0
	v_lshl_add_u64 v[0:1], s[8:9], 0, v[198:199]
	v_add_co_u32_e32 v0, vcc, s90, v0
	global_load_dwordx4 v[64:67], v198, s[8:9]
	global_load_dwordx4 v[168:171], v198, s[8:9] offset:1024
	global_load_dwordx4 v[164:167], v198, s[8:9] offset:2048
	global_load_dwordx4 v[160:163], v198, s[8:9] offset:3072
	v_addc_co_u32_e32 v1, vcc, 0, v1, vcc
	global_load_dwordx4 v[156:159], v[0:1], off
	global_load_dwordx4 v[152:155], v[0:1], off offset:1024
	global_load_dwordx4 v[148:151], v[0:1], off offset:2048
	global_load_dwordx4 v[144:147], v[0:1], off offset:3072
	v_cmp_lt_u32_e32 vcc, 7, v2
	v_mov_b32_e32 v1, v177
	v_mov_b32_e32 v207, 0
	v_cndmask_b32_e32 v0, 0, v3, vcc
	v_add_u32_e32 v201, v0, v172
	v_lshlrev_b32_e32 v0, 14, v4
	v_add_u32_e32 v0, 0xffff0000, v0
	v_lshl_add_u64 v[0:1], s[80:81], 0, v[0:1]
	s_mov_b32 s46, 0
	s_sub_i32 s37, s48, s47
	v_sub_u32_e32 v199, v208, v2
	v_lshl_add_u64 v[204:205], v[174:175], 0, v[0:1]
	v_mov_b32_e32 v206, 0xff61b1e6
	s_mov_b64 s[8:9], 0
	s_mov_b32 s47, 0
	v_mov_b32_e32 v0, 0
	v_mov_b32_e32 v1, v207
	v_mov_b32_e32 v2, v207
	v_mov_b32_e32 v3, v207
	v_mov_b32_e32 v4, v207
	v_mov_b32_e32 v5, v207
	v_mov_b32_e32 v6, v207
	v_mov_b32_e32 v7, v207
	s_waitcnt vmcnt(16)
	v_mov_b32_e32 v8, v207
	v_mov_b32_e32 v9, v207
	v_mov_b32_e32 v10, v207
	v_mov_b32_e32 v11, v207
	v_mov_b32_e32 v12, v207
	v_mov_b32_e32 v13, v207
	v_mov_b32_e32 v14, v207
	v_mov_b32_e32 v15, v207
	v_mov_b32_e32 v16, 0
	v_mov_b32_e32 v17, v207
	v_mov_b32_e32 v18, v207
	v_mov_b32_e32 v19, v207
	v_mov_b32_e32 v20, v207
	v_mov_b32_e32 v21, v207
	v_mov_b32_e32 v22, v207
	v_mov_b32_e32 v23, v207
	v_mov_b32_e32 v24, v207
	v_mov_b32_e32 v25, v207
	v_mov_b32_e32 v26, v207
	v_mov_b32_e32 v27, v207
	v_mov_b32_e32 v28, v207
	v_mov_b32_e32 v29, v207
	v_mov_b32_e32 v30, v207
	v_mov_b32_e32 v31, v207
	v_mov_b32_e32 v32, 0
	v_mov_b32_e32 v33, v207
	v_mov_b32_e32 v34, v207
	v_mov_b32_e32 v35, v207
	v_mov_b32_e32 v36, v207
	v_mov_b32_e32 v37, v207
	v_mov_b32_e32 v38, v207
	v_mov_b32_e32 v39, v207
	v_mov_b32_e32 v40, v207
	v_mov_b32_e32 v41, v207
	v_mov_b32_e32 v42, v207
	v_mov_b32_e32 v43, v207
	v_mov_b32_e32 v44, v207
	v_mov_b32_e32 v45, v207
	v_mov_b32_e32 v46, v207
	v_mov_b32_e32 v47, v207
	v_mov_b32_e32 v48, 0
	v_mov_b32_e32 v49, v207
	v_mov_b32_e32 v50, v207
	v_mov_b32_e32 v51, v207
	v_mov_b32_e32 v52, v207
	v_mov_b32_e32 v53, v207
	v_mov_b32_e32 v54, v207
	v_mov_b32_e32 v55, v207
	v_mov_b32_e32 v56, v207
	v_mov_b32_e32 v57, v207
	v_mov_b32_e32 v58, v207
	v_mov_b32_e32 v59, v207
	v_mov_b32_e32 v60, v207
	v_mov_b32_e32 v61, v207
	v_mov_b32_e32 v62, v207
	v_mov_b32_e32 v63, v207
	s_lshr_b32 s98, s47, 1
	s_add_i32 s98, s98, s37
	s_lshl_b32 s98, s98, 7
	s_ashr_i32 s99, s98, 31
	s_lshl_b64 s[98:99], s[98:99], 2
	s_add_u32 s98, s35, s98
	s_addc_u32 s99, s36, s99
	s_and_b32 s50, s46, 32
	v_add_lshl_u32 v248, s50, v199, 2
	global_load_dwordx4 v[232:235], v248, s[98:99] offset:3584
	global_load_dwordx4 v[236:239], v248, s[98:99] offset:3600
	global_load_dwordx4 v[240:243], v248, s[98:99] offset:3648
	global_load_dwordx4 v[244:247], v248, s[98:99] offset:3664
.LBB0_1293:
	v_mov_b32_e32 v203, v207
	v_mov_b32_e32 v209, v206
	v_lshl_add_u64 v[206:207], v[204:205], 0, s[8:9]
	s_mov_b32 s48, 0x35000000
	v_add_co_u32_e32 v68, vcc, s48, v206
	s_mov_b32 s48, 0x35001000
	s_nop 0
	v_addc_co_u32_e32 v69, vcc, 0, v207, vcc
	v_add_co_u32_e32 v70, vcc, s48, v206
	s_lshr_b32 s48, s47, 1
	s_add_i32 s48, s48, s37
	s_lshl_b32 s48, s48, 7
	s_ashr_i32 s49, s48, 31
	s_lshl_b64 s[48:49], s[48:49], 2
	s_add_u32 s48, s35, s48
	v_addc_co_u32_e32 v71, vcc, 0, v207, vcc
	s_addc_u32 s49, s36, s49
	s_and_b32 s50, s46, 32
	global_load_dwordx4 v[136:139], v[70:71], off offset:-4096
	global_load_dwordx4 v[140:143], v[68:69], off offset:1024
	global_load_dwordx4 v[128:131], v[68:69], off offset:2048
	global_load_dwordx4 v[132:135], v[68:69], off offset:3072
	global_load_dwordx4 v[120:123], v[70:71], off
	global_load_dwordx4 v[124:127], v[70:71], off offset:1024
	global_load_dwordx4 v[112:115], v[70:71], off offset:2048
	global_load_dwordx4 v[116:119], v[70:71], off offset:3072
	s_waitcnt vmcnt(15)
	v_mfma_f32_32x32x16_bf16 v[64:79], v[64:67], v[108:111], 0
	s_movk_i32 s48, 0xffef
	s_add_i32 s47, s47, 1
	s_add_u32 s8, s8, 0x2000
	s_addc_u32 s9, s9, 0
	s_add_i32 s46, s46, 32
	s_waitcnt vmcnt(14)
	v_mfma_f32_32x32x16_bf16 v[64:79], v[168:171], v[104:107], v[64:79]
	s_waitcnt vmcnt(13)
	v_mfma_f32_32x32x16_bf16 v[64:79], v[164:167], v[100:103], v[64:79]
	s_waitcnt vmcnt(12)
	v_mfma_f32_32x32x16_bf16 v[64:79], v[160:163], v[96:99], v[64:79]
	s_waitcnt vmcnt(11)
	v_mfma_f32_32x32x16_bf16 v[64:79], v[156:159], v[92:95], v[64:79]
	v_add_u32_e32 v156, s50, v201
	v_cmp_gt_u32_e32 vcc, 16, v156
	s_waitcnt vmcnt(10)
	v_mfma_f32_32x32x16_bf16 v[64:79], v[152:155], v[88:91], v[64:79]
	s_waitcnt vmcnt(9)
	v_mfma_f32_32x32x16_bf16 v[64:79], v[148:151], v[84:87], v[64:79]
	s_waitcnt vmcnt(8)
	v_mfma_f32_32x32x16_bf16 v[64:79], v[144:147], v[80:83], v[64:79]
	s_nop 3
	s_nop 7
	v_add_f32_e32 v64, v64, v232
	v_cndmask_b32_e32 v217, v222, v64, vcc
	v_add_u32_e32 v64, 1, v156
	v_cmp_gt_u32_e32 vcc, 16, v64
	v_add_f32_e32 v64, v65, v233
	s_nop 0
	v_cndmask_b32_e32 v216, v222, v64, vcc
	v_add_u32_e32 v64, 2, v156
	v_cmp_gt_u32_e32 vcc, 16, v64
	v_add_f32_e32 v64, v66, v234
	s_nop 0
	v_cndmask_b32_e32 v215, v222, v64, vcc
	v_add_u32_e32 v64, 3, v156
	v_cmp_gt_u32_e32 vcc, 16, v64
	v_add_f32_e32 v64, v67, v235
	s_nop 0
	v_cndmask_b32_e32 v214, v222, v64, vcc
	v_add_u32_e32 v64, 4, v156
	v_cmp_gt_u32_e32 vcc, 16, v64
	v_add_f32_e32 v64, v68, v236
	s_nop 0
	v_cndmask_b32_e32 v213, v222, v64, vcc
	v_add_u32_e32 v64, 5, v156
	v_cmp_gt_u32_e32 vcc, 16, v64
	v_add_f32_e32 v64, v69, v237
	s_nop 0
	v_cndmask_b32_e32 v212, v222, v64, vcc
	v_add_u32_e32 v64, 6, v156
	v_cmp_gt_u32_e32 vcc, 16, v64
	v_add_f32_e32 v64, v70, v238
	s_nop 0
	v_cndmask_b32_e32 v211, v222, v64, vcc
	v_add_u32_e32 v64, 7, v156
	v_cmp_gt_u32_e32 vcc, 16, v64
	v_add_f32_e32 v64, v71, v239
	s_nop 0
	v_cndmask_b32_e32 v210, v222, v64, vcc
	v_cmp_lt_u32_e32 vcc, s48, v156
	v_add_f32_e32 v64, v72, v240
	s_mov_b32 s48, 0x33002000
	v_cndmask_b32_e32 v221, v222, v64, vcc
	v_add_u32_e32 v64, 17, v156
	v_cmp_gt_u32_e32 vcc, 16, v64
	v_add_f32_e32 v64, v73, v241
	s_nop 0
	v_cndmask_b32_e32 v220, v222, v64, vcc
	v_add_u32_e32 v64, 18, v156
	v_cmp_gt_u32_e32 vcc, 16, v64
	v_add_f32_e32 v64, v74, v242
	s_nop 0
	v_cndmask_b32_e32 v219, v222, v64, vcc
	v_add_u32_e32 v64, 19, v156
	v_cmp_gt_u32_e32 vcc, 16, v64
	v_add_f32_e32 v64, v75, v243
	s_nop 0
	v_cndmask_b32_e32 v218, v222, v64, vcc
	v_add_u32_e32 v64, 20, v156
	v_cmp_gt_u32_e32 vcc, 16, v64
	v_add_f32_e32 v64, v76, v244
	s_nop 0
	v_cndmask_b32_e32 v75, v222, v64, vcc
	v_add_u32_e32 v64, 21, v156
	v_cmp_gt_u32_e32 vcc, 16, v64
	v_add_f32_e32 v64, v77, v245
	s_nop 0
	v_cndmask_b32_e32 v74, v222, v64, vcc
	v_add_u32_e32 v64, 22, v156
	v_cmp_gt_u32_e32 vcc, 16, v64
	v_add_f32_e32 v64, v78, v246
	s_nop 0
	v_cndmask_b32_e32 v73, v222, v64, vcc
	v_add_u32_e32 v64, 23, v156
	v_cmp_gt_u32_e32 vcc, 16, v64
	v_add_f32_e32 v64, v79, v247
	s_nop 0
	v_cndmask_b32_e32 v72, v222, v64, vcc
	s_lshr_b32 s98, s47, 1
	s_add_i32 s98, s98, s37
	s_lshl_b32 s98, s98, 7
	s_ashr_i32 s99, s98, 31
	s_lshl_b64 s[98:99], s[98:99], 2
	s_add_u32 s98, s35, s98
	s_addc_u32 s99, s36, s99
	s_and_b32 s50, s46, 32
	v_add_lshl_u32 v248, s50, v199, 2
	global_load_dwordx4 v[232:235], v248, s[98:99] offset:3584
	global_load_dwordx4 v[236:239], v248, s[98:99] offset:3600
	global_load_dwordx4 v[240:243], v248, s[98:99] offset:3648
	global_load_dwordx4 v[244:247], v248, s[98:99] offset:3664
	s_cmp_lg_u32 s8, 0x1e000
	v_add_co_u32_e32 v68, vcc, s48, v206
	s_mov_b32 s48, 0x33003000
	s_nop 0
	v_addc_co_u32_e32 v69, vcc, 0, v207, vcc
	v_add_co_u32_e32 v70, vcc, s48, v206
	s_nop 1
	v_addc_co_u32_e32 v71, vcc, 0, v207, vcc
	global_load_dwordx4 v[64:67], v[70:71], off offset:-4096
	global_load_dwordx4 v[168:171], v[68:69], off offset:1024
	global_load_dwordx4 v[164:167], v[68:69], off offset:2048
	global_load_dwordx4 v[160:163], v[68:69], off offset:3072
	global_load_dwordx4 v[156:159], v[70:71], off
	global_load_dwordx4 v[152:155], v[70:71], off offset:1024
	global_load_dwordx4 v[148:151], v[70:71], off offset:2048
	global_load_dwordx4 v[144:147], v[70:71], off offset:3072
	v_max3_f32 v68, v217, s11, v216
	v_max3_f32 v68, v68, v215, v214
	v_max3_f32 v68, v68, v213, v212
	v_max3_f32 v68, v68, v211, v210
	v_max3_f32 v68, v68, v221, v220
	v_max3_f32 v68, v68, v219, v218
	v_mbcnt_lo_u32_b32 v69, -1, 0
	v_mbcnt_hi_u32_b32 v69, -1, v69
	v_max3_f32 v68, v68, v75, v74
	v_lshlrev_b32_e32 v69, 2, v69
	v_max3_f32 v68, v68, v73, v72
	v_xor_b32_e32 v69, 0x80, v69
	ds_bpermute_b32 v69, v69, v68
	s_waitcnt lgkmcnt(0)
	v_max3_f32 v206, v209, v68, v69
	v_sub_f32_e32 v69, v217, v206
	v_exp_f32_e32 v69, v69
	v_sub_f32_e32 v70, v216, v206
	v_exp_f32_e32 v70, v70
	v_sub_f32_e32 v71, v215, v206
	v_exp_f32_e32 v71, v71
	v_sub_f32_e32 v76, v214, v206
	v_exp_f32_e32 v76, v76
	v_sub_f32_e32 v77, v213, v206
	v_sub_f32_e32 v72, v72, v206
	v_exp_f32_e32 v77, v77
	v_sub_f32_e32 v78, v212, v206
	v_exp_f32_e32 v184, v72
	v_add_f32_e32 v72, 0, v69
	v_exp_f32_e32 v78, v78
	v_sub_f32_e32 v79, v211, v206
	v_add_f32_e32 v72, v70, v72
	v_exp_f32_e32 v79, v79
	v_sub_f32_e32 v178, v210, v206
	v_add_f32_e32 v72, v71, v72
	v_exp_f32_e32 v178, v178
	v_sub_f32_e32 v179, v221, v206
	v_add_f32_e32 v72, v76, v72
	v_exp_f32_e32 v179, v179
	v_sub_f32_e32 v180, v220, v206
	v_add_f32_e32 v72, v77, v72
	v_exp_f32_e32 v180, v180
	v_sub_f32_e32 v181, v219, v206
	v_add_f32_e32 v72, v78, v72
	v_exp_f32_e32 v181, v181
	v_sub_f32_e32 v182, v218, v206
	v_add_f32_e32 v72, v79, v72
	v_exp_f32_e32 v182, v182
	v_sub_f32_e32 v75, v75, v206
	v_add_f32_e32 v72, v178, v72
	v_exp_f32_e32 v75, v75
	v_sub_f32_e32 v74, v74, v206
	v_add_f32_e32 v72, v179, v72
	v_exp_f32_e32 v74, v74
	v_sub_f32_e32 v73, v73, v206
	v_add_f32_e32 v72, v180, v72
	v_exp_f32_e32 v183, v73
	v_add_f32_e32 v72, v181, v72
	v_add_f32_e32 v72, v182, v72
	v_sub_f32_e32 v68, v209, v206
	v_add_f32_e32 v72, v75, v72
	v_exp_f32_e32 v68, v68
	v_add_f32_e32 v72, v74, v72
	v_add_f32_e32 v72, v183, v72
	v_add_f32_e32 v207, v184, v72
	v_bfe_u32 v72, v178, 16, 1
	v_bfe_u32 v73, v78, 16, 1
	v_bfe_u32 v185, v76, 16, 1
	v_bfe_u32 v186, v70, 16, 1
	v_add3_u32 v70, v70, v186, s25
	v_add3_u32 v76, v76, v185, s25
	v_add3_u32 v78, v78, v73, s25
	v_add3_u32 v72, v178, v72, s25
	v_bfe_u32 v73, v69, 16, 1
	v_bfe_u32 v178, v71, 16, 1
	v_bfe_u32 v185, v77, 16, 1
	v_bfe_u32 v186, v79, 16, 1
	v_pk_mul_f32 v[62:63], v[62:63], v[68:69] op_sel_hi:[1,0]
	v_pk_mul_f32 v[60:61], v[60:61], v[68:69] op_sel_hi:[1,0]
	v_pk_mul_f32 v[58:59], v[58:59], v[68:69] op_sel_hi:[1,0]
	v_pk_mul_f32 v[56:57], v[56:57], v[68:69] op_sel_hi:[1,0]
	v_pk_mul_f32 v[54:55], v[54:55], v[68:69] op_sel_hi:[1,0]
	v_pk_mul_f32 v[52:53], v[52:53], v[68:69] op_sel_hi:[1,0]
	v_pk_mul_f32 v[50:51], v[50:51], v[68:69] op_sel_hi:[1,0]
	v_pk_mul_f32 v[48:49], v[48:49], v[68:69] op_sel_hi:[1,0]
	v_pk_mul_f32 v[46:47], v[46:47], v[68:69] op_sel_hi:[1,0]
	v_pk_mul_f32 v[44:45], v[44:45], v[68:69] op_sel_hi:[1,0]
	v_pk_mul_f32 v[42:43], v[42:43], v[68:69] op_sel_hi:[1,0]
	v_pk_mul_f32 v[40:41], v[40:41], v[68:69] op_sel_hi:[1,0]
	v_pk_mul_f32 v[38:39], v[38:39], v[68:69] op_sel_hi:[1,0]
	v_pk_mul_f32 v[36:37], v[36:37], v[68:69] op_sel_hi:[1,0]
	v_pk_mul_f32 v[34:35], v[34:35], v[68:69] op_sel_hi:[1,0]
	v_pk_mul_f32 v[32:33], v[32:33], v[68:69] op_sel_hi:[1,0]
	v_pk_mul_f32 v[30:31], v[30:31], v[68:69] op_sel_hi:[1,0]
	v_pk_mul_f32 v[28:29], v[28:29], v[68:69] op_sel_hi:[1,0]
	v_pk_mul_f32 v[26:27], v[26:27], v[68:69] op_sel_hi:[1,0]
	v_pk_mul_f32 v[24:25], v[24:25], v[68:69] op_sel_hi:[1,0]
	v_pk_mul_f32 v[22:23], v[22:23], v[68:69] op_sel_hi:[1,0]
	v_pk_mul_f32 v[20:21], v[20:21], v[68:69] op_sel_hi:[1,0]
	v_pk_mul_f32 v[18:19], v[18:19], v[68:69] op_sel_hi:[1,0]
	v_pk_mul_f32 v[16:17], v[16:17], v[68:69] op_sel_hi:[1,0]
	v_pk_mul_f32 v[14:15], v[14:15], v[68:69] op_sel_hi:[1,0]
	v_pk_mul_f32 v[12:13], v[12:13], v[68:69] op_sel_hi:[1,0]
	v_pk_mul_f32 v[10:11], v[10:11], v[68:69] op_sel_hi:[1,0]
	v_pk_mul_f32 v[8:9], v[8:9], v[68:69] op_sel_hi:[1,0]
	v_pk_mul_f32 v[6:7], v[6:7], v[68:69] op_sel_hi:[1,0]
	v_pk_mul_f32 v[4:5], v[4:5], v[68:69] op_sel_hi:[1,0]
	v_pk_mul_f32 v[2:3], v[2:3], v[68:69] op_sel_hi:[1,0]
	v_pk_mul_f32 v[0:1], v[0:1], v[68:69] op_sel_hi:[1,0]
	v_add3_u32 v79, v79, v186, s25
	v_add3_u32 v77, v77, v185, s25
	v_add3_u32 v71, v71, v178, s25
	v_add3_u32 v69, v69, v73, s25
	v_lshrrev_b32_e32 v69, 16, v69
	v_lshrrev_b32_e32 v71, 16, v71
	v_lshrrev_b32_e32 v77, 16, v77
	v_lshrrev_b32_e32 v73, 16, v79
	v_and_or_b32 v73, v72, s10, v73
	v_and_or_b32 v72, v78, s10, v77
	v_and_or_b32 v71, v76, s10, v71
	v_and_or_b32 v70, v70, s10, v69
	v_bfe_u32 v76, v74, 16, 1
	v_bfe_u32 v77, v182, 16, 1
	s_waitcnt vmcnt(12)
	v_mfma_f32_32x32x16_bf16 v[48:63], v[136:139], v[70:73], v[48:63]
	v_bfe_u32 v78, v180, 16, 1
	v_add3_u32 v78, v180, v78, s25
	v_add3_u32 v79, v182, v77, s25
	v_add3_u32 v74, v74, v76, s25
	v_bfe_u32 v76, v179, 16, 1
	v_bfe_u32 v77, v181, 16, 1
	v_bfe_u32 v178, v75, 16, 1
	v_mfma_f32_32x32x16_bf16 v[32:47], v[128:131], v[70:73], v[32:47]
	v_bfe_u32 v180, v183, 16, 1
	v_bfe_u32 v69, v184, 16, 1
	v_add3_u32 v180, v183, v180, s25
	v_add3_u32 v75, v75, v178, s25
	v_add3_u32 v77, v181, v77, s25
	v_add3_u32 v76, v179, v76, s25
	v_add3_u32 v69, v184, v69, s25
	v_mfma_f32_32x32x16_bf16 v[16:31], v[120:123], v[70:73], v[16:31]
	v_lshrrev_b32_e32 v178, 16, v76
	v_lshrrev_b32_e32 v179, 16, v77
	v_lshrrev_b32_e32 v75, 16, v75
	v_lshrrev_b32_e32 v76, 16, v180
	v_and_or_b32 v77, v69, s10, v76
	v_and_or_b32 v76, v74, s10, v75
	v_and_or_b32 v75, v79, s10, v179
	v_mfma_f32_32x32x16_bf16 v[0:15], v[112:115], v[70:73], v[0:15]
	v_and_or_b32 v74, v78, s10, v178
	v_fmac_f32_e32 v207, v203, v68
	s_nop 0
	v_mfma_f32_32x32x16_bf16 v[48:63], v[140:143], v[74:77], v[48:63]
	v_mfma_f32_32x32x16_bf16 v[32:47], v[132:135], v[74:77], v[32:47]
	v_mfma_f32_32x32x16_bf16 v[16:31], v[124:127], v[74:77], v[16:31]
	v_mfma_f32_32x32x16_bf16 v[0:15], v[116:119], v[74:77], v[0:15]
	s_cbranch_scc1 .LBB0_1293
	s_waitcnt vmcnt(7)
	v_mfma_f32_32x32x16_bf16 v[64:79], v[64:67], v[108:111], 0
	s_lshl_b32 s3, s3, 1
	s_add_u32 s3, s28, s3
	s_addc_u32 s8, s29, 0
	s_mul_hi_i32 s9, s2, 0x1400
	s_mulk_i32 s2, 0x1400
	s_add_u32 s46, s18, s2
	s_addc_u32 s9, s19, s9
	s_lshl_b64 s[0:1], s[0:1], 1
	s_add_u32 s2, s3, s0
	s_waitcnt vmcnt(6)
	v_mfma_f32_32x32x16_bf16 v[64:79], v[168:171], v[104:107], v[64:79]
	s_addc_u32 s3, s8, s1
	s_lshl_b32 s0, s34, 1
	s_add_u32 s0, s46, s0
	s_addc_u32 s1, s9, 0
	s_lshl_b32 s8, s37, 7
	s_addk_i32 s8, 0x700
	s_ashr_i32 s9, s8, 31
	s_lshl_b64 s[8:9], s[8:9], 2
	s_add_u32 s8, s35, s8
	s_addc_u32 s9, s36, s9
	s_waitcnt vmcnt(5)
	v_mfma_f32_32x32x16_bf16 v[64:79], v[164:167], v[100:103], v[64:79]
	v_lshlrev_b32_e32 v100, 2, v199
	global_load_dwordx4 v[120:123], v100, s[8:9] offset:144
	global_load_dwordx4 v[124:127], v100, s[8:9] offset:128
	global_load_dwordx4 v[116:119], v100, s[8:9] offset:208
	global_load_dwordx4 v[128:131], v100, s[8:9] offset:192
	v_mov_b32_e32 v199, v177
	v_add_u32_e32 v132, 32, v201
	v_add_u32_e32 v133, 33, v201
	v_add_u32_e32 v134, 34, v201
	s_waitcnt vmcnt(8)
	v_mfma_f32_32x32x16_bf16 v[64:79], v[160:163], v[96:99], v[64:79]
	v_add_u32_e32 v135, 35, v201
	v_add_u32_e32 v136, 36, v201
	v_add_u32_e32 v137, 37, v201
	v_add_u32_e32 v138, 38, v201
	v_add_u32_e32 v139, 39, v201
	v_mov_b32_e32 v203, v177
	s_add_i32 s33, s33, s5
	s_waitcnt vmcnt(7)
	v_mfma_f32_32x32x16_bf16 v[64:79], v[156:159], v[92:95], v[64:79]
	v_lshl_add_u64 v[92:93], s[2:3], 0, v[198:199]
	s_mov_b32 s2, 0x1f000
	v_add_co_u32_e32 v100, vcc, s2, v92
	s_mov_b32 s2, 0x1e000
	s_nop 0
	v_addc_co_u32_e32 v101, vcc, 0, v93, vcc
	s_waitcnt vmcnt(6)
	v_mfma_f32_32x32x16_bf16 v[64:79], v[152:155], v[88:91], v[64:79]
	v_add_co_u32_e32 v102, vcc, s2, v92
	s_cmpk_gt_i32 s33, 0xfff
	s_nop 0
	v_addc_co_u32_e32 v103, vcc, 0, v93, vcc
	v_cmp_gt_u32_e32 vcc, 16, v132
	s_waitcnt vmcnt(5)
	v_mfma_f32_32x32x16_bf16 v[64:79], v[148:151], v[84:87], v[64:79]
	global_load_dwordx4 v[108:111], v[102:103], off offset:1024
	global_load_dwordx4 v[104:107], v[102:103], off offset:2048
	global_load_dwordx4 v[96:99], v[100:101], off
	global_load_dwordx4 v[92:95], v[100:101], off offset:1024
	global_load_dwordx4 v[88:91], v[100:101], off offset:2048
	global_load_dwordx4 v[84:87], v[100:101], off offset:3072
	global_load_dwordx4 v[112:115], v[100:101], off offset:-4096
	s_nop 0
	global_load_dwordx4 v[100:103], v[102:103], off offset:3072
	s_waitcnt vmcnt(12)
	v_mfma_f32_32x32x16_bf16 v[64:79], v[144:147], v[80:83], v[64:79]
	s_waitcnt vmcnt(11)
	v_mov_b32_e32 v80, v122
	s_waitcnt vmcnt(10)
	v_mov_b32_e32 v81, v127
	v_mov_b32_e32 v82, v121
	v_mov_b32_e32 v83, v124
	v_mov_b32_e32 v121, v123
	v_mov_b32_e32 v122, v126
	s_waitcnt vmcnt(8)
	v_mov_b32_e32 v123, v129
	s_nop 1
	v_add_f32_e32 v64, v64, v83
	v_add_f32_e32 v65, v65, v125
	v_cndmask_b32_e32 v64, v222, v64, vcc
	v_cmp_gt_u32_e32 vcc, 16, v133
	v_add_f32_e32 v66, v66, v122
	v_add_f32_e32 v67, v67, v81
	v_cndmask_b32_e32 v65, v222, v65, vcc
	v_cmp_gt_u32_e32 vcc, 16, v134
	v_add_f32_e32 v68, v68, v120
	v_add_f32_e32 v69, v69, v82
	v_cndmask_b32_e32 v66, v222, v66, vcc
	v_cmp_gt_u32_e32 vcc, 16, v135
	v_add_f32_e32 v70, v70, v80
	v_mov_b32_e32 v124, v131
	v_cndmask_b32_e32 v67, v222, v67, vcc
	v_cmp_gt_u32_e32 vcc, 16, v136
	v_mov_b32_e32 v126, v128
	v_add_f32_e32 v71, v71, v121
	v_cndmask_b32_e32 v68, v222, v68, vcc
	v_cmp_gt_u32_e32 vcc, 16, v137
	v_add_u32_e32 v80, 49, v201
	v_add_f32_e32 v72, v72, v126
	v_cndmask_b32_e32 v69, v222, v69, vcc
	v_cmp_gt_u32_e32 vcc, 16, v138
	v_add_f32_e32 v73, v73, v123
	v_add_f32_e32 v74, v74, v130
	v_cndmask_b32_e32 v70, v222, v70, vcc
	v_cmp_gt_u32_e32 vcc, 16, v139
	v_add_f32_e32 v75, v75, v124
	v_add_f32_e32 v76, v76, v116
	v_cndmask_b32_e32 v71, v222, v71, vcc
	v_cmp_lt_u32_e32 vcc, 48, v132
	v_add_f32_e32 v77, v77, v117
	v_add_f32_e32 v78, v78, v118
	v_cndmask_b32_e32 v72, v222, v72, vcc
	v_cmp_gt_u32_e32 vcc, 16, v80
	v_add_u32_e32 v80, 50, v201
	v_add_f32_e32 v79, v79, v119
	v_cndmask_b32_e32 v73, v222, v73, vcc
	v_cmp_gt_u32_e32 vcc, 16, v80
	v_add_u32_e32 v80, 51, v201
	v_mbcnt_lo_u32_b32 v81, -1, 0
	v_mbcnt_hi_u32_b32 v81, -1, v81
	s_nop 0
	v_cndmask_b32_e32 v74, v222, v74, vcc
	v_cmp_gt_u32_e32 vcc, 16, v80
	v_add_u32_e32 v80, 52, v201
	v_lshlrev_b32_e32 v81, 2, v81
	v_cndmask_b32_e32 v75, v222, v75, vcc
	v_cmp_gt_u32_e32 vcc, 16, v80
	v_add_u32_e32 v80, 53, v201
	v_xor_b32_e32 v81, 0x80, v81
	v_cndmask_b32_e32 v76, v222, v76, vcc
	v_cmp_gt_u32_e32 vcc, 16, v80
	v_add_u32_e32 v80, 54, v201
	s_nop 0
	v_cndmask_b32_e32 v77, v222, v77, vcc
	v_cmp_gt_u32_e32 vcc, 16, v80
	v_add_u32_e32 v80, 55, v201
	v_mov_b32_e32 v201, v177
	v_cndmask_b32_e32 v78, v222, v78, vcc
	v_cmp_gt_u32_e32 vcc, 16, v80
	v_max3_f32 v80, v64, s11, v65
	v_max3_f32 v80, v80, v66, v67
	v_max3_f32 v80, v80, v68, v69
	v_max3_f32 v80, v80, v70, v71
	v_max3_f32 v80, v80, v72, v73
	v_max3_f32 v80, v80, v74, v75
	v_cndmask_b32_e32 v79, v222, v79, vcc
	v_max3_f32 v80, v80, v76, v77
	v_max3_f32 v80, v80, v78, v79
	ds_bpermute_b32 v81, v81, v80
	s_waitcnt lgkmcnt(0)
	v_max3_f32 v80, v206, v80, v81
	v_sub_f32_e32 v64, v64, v80
	v_exp_f32_e32 v82, v64
	v_sub_f32_e32 v64, v65, v80
	v_exp_f32_e32 v65, v64
	v_sub_f32_e32 v64, v66, v80
	v_exp_f32_e32 v83, v64
	v_sub_f32_e32 v64, v67, v80
	v_exp_f32_e32 v116, v64
	v_sub_f32_e32 v64, v68, v80
	v_exp_f32_e32 v117, v64
	v_sub_f32_e32 v64, v69, v80
	v_exp_f32_e32 v118, v64
	v_sub_f32_e32 v64, v70, v80
	v_exp_f32_e32 v119, v64
	v_sub_f32_e32 v64, v71, v80
	v_exp_f32_e32 v120, v64
	v_sub_f32_e32 v64, v72, v80
	v_exp_f32_e32 v121, v64
	v_sub_f32_e32 v64, v73, v80
	v_exp_f32_e32 v122, v64
	v_sub_f32_e32 v64, v74, v80
	v_exp_f32_e32 v74, v64
	v_sub_f32_e32 v64, v75, v80
	v_exp_f32_e32 v75, v64
	v_sub_f32_e32 v64, v76, v80
	v_sub_f32_e32 v66, v78, v80
	v_sub_f32_e32 v81, v206, v80
	v_exp_f32_e32 v76, v64
	v_sub_f32_e32 v64, v77, v80
	v_exp_f32_e32 v78, v66
	v_sub_f32_e32 v66, v79, v80
	v_bfe_u32 v68, v116, 16, 1
	v_bfe_u32 v69, v65, 16, 1
	v_exp_f32_e32 v77, v64
	v_exp_f32_e32 v64, v81
	v_exp_f32_e32 v79, v66
	v_add3_u32 v70, v65, v69, s25
	v_add3_u32 v71, v116, v68, s25
	v_bfe_u32 v68, v82, 16, 1
	v_bfe_u32 v69, v83, 16, 1
	v_bfe_u32 v72, v117, 16, 1
	v_bfe_u32 v73, v119, 16, 1
	v_bfe_u32 v66, v120, 16, 1
	v_bfe_u32 v67, v118, 16, 1
	v_add3_u32 v73, v119, v73, s25
	v_add3_u32 v72, v117, v72, s25
	v_add3_u32 v69, v83, v69, s25
	v_add3_u32 v68, v82, v68, s25
	v_add3_u32 v67, v118, v67, s25
	v_add3_u32 v66, v120, v66, s25
	v_lshrrev_b32_e32 v80, 16, v68
	v_lshrrev_b32_e32 v81, 16, v69
	v_lshrrev_b32_e32 v68, 16, v72
	v_lshrrev_b32_e32 v69, 16, v73
	v_bfe_u32 v72, v75, 16, 1
	v_bfe_u32 v73, v122, 16, 1
	v_and_or_b32 v69, v66, s10, v69
	v_and_or_b32 v68, v67, s10, v68
	v_and_or_b32 v67, v71, s10, v81
	v_and_or_b32 v66, v70, s10, v80
	v_add3_u32 v80, v122, v73, s25
	v_add3_u32 v81, v75, v72, s25
	v_bfe_u32 v72, v121, 16, 1
	v_bfe_u32 v73, v74, 16, 1
	v_bfe_u32 v124, v78, 16, 1
	v_pk_mul_f32 v[62:63], v[62:63], v[64:65] op_sel_hi:[1,0]
	v_pk_mul_f32 v[60:61], v[60:61], v[64:65] op_sel_hi:[1,0]
	v_pk_mul_f32 v[58:59], v[58:59], v[64:65] op_sel_hi:[1,0]
	v_pk_mul_f32 v[56:57], v[56:57], v[64:65] op_sel_hi:[1,0]
	v_pk_mul_f32 v[54:55], v[54:55], v[64:65] op_sel_hi:[1,0]
	v_pk_mul_f32 v[52:53], v[52:53], v[64:65] op_sel_hi:[1,0]
	v_pk_mul_f32 v[50:51], v[50:51], v[64:65] op_sel_hi:[1,0]
	v_pk_mul_f32 v[48:49], v[48:49], v[64:65] op_sel_hi:[1,0]
	v_bfe_u32 v70, v79, 16, 1
	v_add3_u32 v124, v78, v124, s25
	v_add3_u32 v73, v74, v73, s25
	v_add3_u32 v72, v121, v72, s25
	v_add3_u32 v70, v79, v70, s25
	v_lshrrev_b32_e32 v125, 16, v72
	s_waitcnt vmcnt(1)
	v_mfma_f32_32x32x16_bf16 v[48:63], v[112:115], v[66:69], v[48:63]
	v_lshrrev_b32_e32 v112, 16, v73
	v_lshrrev_b32_e32 v73, 16, v124
	v_and_or_b32 v73, v70, s10, v73
	v_and_or_b32 v70, v80, s10, v125
	v_add_f32_e32 v80, 0, v82
	v_pk_mul_f32 v[46:47], v[46:47], v[64:65] op_sel_hi:[1,0]
	v_pk_mul_f32 v[44:45], v[44:45], v[64:65] op_sel_hi:[1,0]
	v_pk_mul_f32 v[42:43], v[42:43], v[64:65] op_sel_hi:[1,0]
	v_pk_mul_f32 v[40:41], v[40:41], v[64:65] op_sel_hi:[1,0]
	v_pk_mul_f32 v[38:39], v[38:39], v[64:65] op_sel_hi:[1,0]
	v_pk_mul_f32 v[36:37], v[36:37], v[64:65] op_sel_hi:[1,0]
	v_pk_mul_f32 v[34:35], v[34:35], v[64:65] op_sel_hi:[1,0]
	v_pk_mul_f32 v[32:33], v[32:33], v[64:65] op_sel_hi:[1,0]
	v_pk_mul_f32 v[30:31], v[30:31], v[64:65] op_sel_hi:[1,0]
	v_pk_mul_f32 v[28:29], v[28:29], v[64:65] op_sel_hi:[1,0]
	v_pk_mul_f32 v[26:27], v[26:27], v[64:65] op_sel_hi:[1,0]
	v_pk_mul_f32 v[24:25], v[24:25], v[64:65] op_sel_hi:[1,0]
	v_pk_mul_f32 v[22:23], v[22:23], v[64:65] op_sel_hi:[1,0]
	v_pk_mul_f32 v[20:21], v[20:21], v[64:65] op_sel_hi:[1,0]
	v_pk_mul_f32 v[18:19], v[18:19], v[64:65] op_sel_hi:[1,0]
	v_pk_mul_f32 v[16:17], v[16:17], v[64:65] op_sel_hi:[1,0]
	v_pk_mul_f32 v[14:15], v[14:15], v[64:65] op_sel_hi:[1,0]
	v_pk_mul_f32 v[12:13], v[12:13], v[64:65] op_sel_hi:[1,0]
	v_pk_mul_f32 v[10:11], v[10:11], v[64:65] op_sel_hi:[1,0]
	v_pk_mul_f32 v[8:9], v[8:9], v[64:65] op_sel_hi:[1,0]
	v_pk_mul_f32 v[6:7], v[6:7], v[64:65] op_sel_hi:[1,0]
	v_pk_mul_f32 v[4:5], v[4:5], v[64:65] op_sel_hi:[1,0]
	v_pk_mul_f32 v[2:3], v[2:3], v[64:65] op_sel_hi:[1,0]
	v_pk_mul_f32 v[0:1], v[0:1], v[64:65] op_sel_hi:[1,0]
	v_add_f32_e32 v65, v65, v80
	v_add_f32_e32 v65, v83, v65
	v_add_f32_e32 v65, v116, v65
	v_add_f32_e32 v65, v117, v65
	v_add_f32_e32 v65, v118, v65
	v_add_f32_e32 v65, v119, v65
	v_add_f32_e32 v65, v120, v65
	v_add_f32_e32 v65, v121, v65
	v_add_f32_e32 v65, v122, v65
	v_add_f32_e32 v65, v74, v65
	v_add_f32_e32 v65, v75, v65
	v_add_f32_e32 v65, v76, v65
	v_add_f32_e32 v65, v77, v65
	v_add_f32_e32 v65, v78, v65
	v_add_f32_e32 v65, v79, v65
	v_fmac_f32_e32 v65, v207, v64
	v_mbcnt_lo_u32_b32 v64, -1, 0
	v_mbcnt_hi_u32_b32 v64, -1, v64
	v_bfe_u32 v123, v76, 16, 1
	v_lshlrev_b32_e32 v64, 2, v64
	v_xor_b32_e32 v64, 0x80, v64
	ds_bpermute_b32 v64, v64, v65
	v_bfe_u32 v71, v77, 16, 1
	v_add3_u32 v123, v76, v123, s25
	v_mfma_f32_32x32x16_bf16 v[32:47], v[104:107], v[66:69], v[32:47]
	v_add3_u32 v71, v77, v71, s25
	s_waitcnt lgkmcnt(0)
	v_add_f32_e32 v64, v65, v64
	v_div_scale_f32 v65, s[2:3], v64, v64, 1.0
	v_lshrrev_b32_e32 v72, 16, v123
	v_and_or_b32 v72, v71, s10, v72
	v_and_or_b32 v71, v81, s10, v112
	v_mfma_f32_32x32x16_bf16 v[16:31], v[96:99], v[66:69], v[16:31]
	v_mfma_f32_32x32x16_bf16 v[0:15], v[88:91], v[66:69], v[0:15]
	v_rcp_f32_e32 v66, v65
	s_nop 0
	v_fma_f32 v67, -v65, v66, 1.0
	v_fmac_f32_e32 v66, v67, v66
	v_div_scale_f32 v67, vcc, 1.0, v64, 1.0
	v_mfma_f32_32x32x16_bf16 v[48:63], v[108:111], v[70:73], v[48:63]
	v_mul_f32_e32 v68, v67, v66
	v_fma_f32 v69, -v65, v68, v67
	v_fmac_f32_e32 v68, v69, v66
	v_fma_f32 v65, -v65, v68, v67
	v_div_fmas_f32 v65, v65, v66, v68
	v_div_fixup_f32 v66, v65, v64, 1.0
	v_lshl_add_u64 v[64:65], s[0:1], 0, v[200:201]
	s_nop 4
	v_mov_b32_e32 v68, v48
	v_mov_b32_e32 v69, v50
	v_pk_mul_f32 v[68:69], v[68:69], v[66:67] op_sel_hi:[1,0]
	v_mov_b32_e32 v50, v49
	v_pk_mul_f32 v[48:49], v[50:51], v[66:67] op_sel_hi:[1,0]
	v_and_b32_sdwa v51, v68, v231 dst_sel:DWORD dst_unused:UNUSED_PAD src0_sel:WORD_1 src1_sel:DWORD
	v_add3_u32 v51, v68, v51, s25
	v_and_b32_sdwa v67, v49, v231 dst_sel:DWORD dst_unused:UNUSED_PAD src0_sel:WORD_1 src1_sel:DWORD
	v_and_b32_sdwa v68, v48, v231 dst_sel:DWORD dst_unused:UNUSED_PAD src0_sel:WORD_1 src1_sel:DWORD
	v_and_b32_sdwa v50, v69, v231 dst_sel:DWORD dst_unused:UNUSED_PAD src0_sel:WORD_1 src1_sel:DWORD
	v_add3_u32 v49, v49, v67, s25
	v_add3_u32 v48, v48, v68, s25
	v_add3_u32 v50, v69, v50, s25
	v_and_b32_e32 v49, 0xffff0000, v49
	v_and_b32_e32 v48, 0xffff0000, v48
	v_lshl_add_u64 v[64:65], v[64:65], 0, v[202:203]
	v_or_b32_sdwa v49, v49, v50 dst_sel:DWORD dst_unused:UNUSED_PAD src0_sel:DWORD src1_sel:WORD_1
	v_or_b32_sdwa v48, v48, v51 dst_sel:DWORD dst_unused:UNUSED_PAD src0_sel:DWORD src1_sel:WORD_1
	global_store_dwordx2 v[64:65], v[48:49], off
	v_mov_b32_e32 v48, v52
	v_mov_b32_e32 v49, v54
	v_pk_mul_f32 v[48:49], v[48:49], v[66:67] op_sel_hi:[1,0]
	v_mov_b32_e32 v54, v53
	v_pk_mul_f32 v[50:51], v[54:55], v[66:67] op_sel_hi:[1,0]
	v_and_b32_sdwa v52, v49, v231 dst_sel:DWORD dst_unused:UNUSED_PAD src0_sel:WORD_1 src1_sel:DWORD
	v_and_b32_sdwa v53, v48, v231 dst_sel:DWORD dst_unused:UNUSED_PAD src0_sel:WORD_1 src1_sel:DWORD
	v_add3_u32 v48, v48, v53, s25
	v_add3_u32 v49, v49, v52, s25
	v_and_b32_sdwa v52, v51, v231 dst_sel:DWORD dst_unused:UNUSED_PAD src0_sel:WORD_1 src1_sel:DWORD
	v_and_b32_sdwa v53, v50, v231 dst_sel:DWORD dst_unused:UNUSED_PAD src0_sel:WORD_1 src1_sel:DWORD
	v_add3_u32 v51, v51, v52, s25
	v_add3_u32 v50, v50, v53, s25
	v_and_b32_e32 v51, 0xffff0000, v51
	v_and_b32_e32 v50, 0xffff0000, v50
	v_or_b32_sdwa v49, v51, v49 dst_sel:DWORD dst_unused:UNUSED_PAD src0_sel:DWORD src1_sel:WORD_1
	v_or_b32_sdwa v48, v50, v48 dst_sel:DWORD dst_unused:UNUSED_PAD src0_sel:DWORD src1_sel:WORD_1
	global_store_dwordx2 v[64:65], v[48:49], off offset:16
	v_mov_b32_e32 v48, v56
	v_mov_b32_e32 v49, v58
	v_pk_mul_f32 v[48:49], v[48:49], v[66:67] op_sel_hi:[1,0]
	v_mov_b32_e32 v58, v57
	v_pk_mul_f32 v[50:51], v[58:59], v[66:67] op_sel_hi:[1,0]
	v_and_b32_sdwa v52, v49, v231 dst_sel:DWORD dst_unused:UNUSED_PAD src0_sel:WORD_1 src1_sel:DWORD
	v_and_b32_sdwa v53, v48, v231 dst_sel:DWORD dst_unused:UNUSED_PAD src0_sel:WORD_1 src1_sel:DWORD
	v_add3_u32 v48, v48, v53, s25
	v_add3_u32 v49, v49, v52, s25
	v_and_b32_sdwa v52, v51, v231 dst_sel:DWORD dst_unused:UNUSED_PAD src0_sel:WORD_1 src1_sel:DWORD
	v_and_b32_sdwa v53, v50, v231 dst_sel:DWORD dst_unused:UNUSED_PAD src0_sel:WORD_1 src1_sel:DWORD
	v_add3_u32 v51, v51, v52, s25
	v_add3_u32 v50, v50, v53, s25
	v_and_b32_e32 v51, 0xffff0000, v51
	v_and_b32_e32 v50, 0xffff0000, v50
	s_waitcnt vmcnt(2)
	v_mfma_f32_32x32x16_bf16 v[32:47], v[100:103], v[70:73], v[32:47]
	v_or_b32_sdwa v49, v51, v49 dst_sel:DWORD dst_unused:UNUSED_PAD src0_sel:DWORD src1_sel:WORD_1
	v_or_b32_sdwa v48, v50, v48 dst_sel:DWORD dst_unused:UNUSED_PAD src0_sel:DWORD src1_sel:WORD_1
	global_store_dwordx2 v[64:65], v[48:49], off offset:32
	v_mov_b32_e32 v48, v60
	v_mov_b32_e32 v49, v62
	v_pk_mul_f32 v[48:49], v[48:49], v[66:67] op_sel_hi:[1,0]
	v_mov_b32_e32 v62, v61
	v_pk_mul_f32 v[50:51], v[62:63], v[66:67] op_sel_hi:[1,0]
	v_and_b32_sdwa v52, v49, v231 dst_sel:DWORD dst_unused:UNUSED_PAD src0_sel:WORD_1 src1_sel:DWORD
	v_and_b32_sdwa v53, v48, v231 dst_sel:DWORD dst_unused:UNUSED_PAD src0_sel:WORD_1 src1_sel:DWORD
	v_add3_u32 v48, v48, v53, s25
	v_add3_u32 v49, v49, v52, s25
	v_and_b32_sdwa v52, v51, v231 dst_sel:DWORD dst_unused:UNUSED_PAD src0_sel:WORD_1 src1_sel:DWORD
	v_and_b32_sdwa v53, v50, v231 dst_sel:DWORD dst_unused:UNUSED_PAD src0_sel:WORD_1 src1_sel:DWORD
	v_add3_u32 v51, v51, v52, s25
	v_add3_u32 v50, v50, v53, s25
	v_and_b32_e32 v51, 0xffff0000, v51
	v_and_b32_e32 v50, 0xffff0000, v50
	v_or_b32_sdwa v49, v51, v49 dst_sel:DWORD dst_unused:UNUSED_PAD src0_sel:DWORD src1_sel:WORD_1
	v_or_b32_sdwa v48, v50, v48 dst_sel:DWORD dst_unused:UNUSED_PAD src0_sel:DWORD src1_sel:WORD_1
	global_store_dwordx2 v[64:65], v[48:49], off offset:48
	v_mov_b32_e32 v48, v32
	v_mov_b32_e32 v49, v34
	v_pk_mul_f32 v[48:49], v[48:49], v[66:67] op_sel_hi:[1,0]
	v_mov_b32_e32 v34, v33
	v_pk_mul_f32 v[32:33], v[34:35], v[66:67] op_sel_hi:[1,0]
	v_and_b32_sdwa v34, v49, v231 dst_sel:DWORD dst_unused:UNUSED_PAD src0_sel:WORD_1 src1_sel:DWORD
	v_and_b32_sdwa v35, v48, v231 dst_sel:DWORD dst_unused:UNUSED_PAD src0_sel:WORD_1 src1_sel:DWORD
	v_add3_u32 v35, v48, v35, s25
	v_add3_u32 v34, v49, v34, s25
	v_and_b32_sdwa v48, v33, v231 dst_sel:DWORD dst_unused:UNUSED_PAD src0_sel:WORD_1 src1_sel:DWORD
	v_and_b32_sdwa v49, v32, v231 dst_sel:DWORD dst_unused:UNUSED_PAD src0_sel:WORD_1 src1_sel:DWORD
	v_add3_u32 v33, v33, v48, s25
	v_add3_u32 v32, v32, v49, s25
	v_and_b32_e32 v33, 0xffff0000, v33
	v_and_b32_e32 v32, 0xffff0000, v32
	v_or_b32_sdwa v33, v33, v34 dst_sel:DWORD dst_unused:UNUSED_PAD src0_sel:DWORD src1_sel:WORD_1
	v_or_b32_sdwa v32, v32, v35 dst_sel:DWORD dst_unused:UNUSED_PAD src0_sel:DWORD src1_sel:WORD_1
	global_store_dwordx2 v[64:65], v[32:33], off offset:64
	v_mov_b32_e32 v32, v36
	v_mov_b32_e32 v33, v38
	v_pk_mul_f32 v[32:33], v[32:33], v[66:67] op_sel_hi:[1,0]
	v_mov_b32_e32 v38, v37
	v_pk_mul_f32 v[34:35], v[38:39], v[66:67] op_sel_hi:[1,0]
	v_and_b32_sdwa v36, v33, v231 dst_sel:DWORD dst_unused:UNUSED_PAD src0_sel:WORD_1 src1_sel:DWORD
	v_and_b32_sdwa v37, v32, v231 dst_sel:DWORD dst_unused:UNUSED_PAD src0_sel:WORD_1 src1_sel:DWORD
	v_add3_u32 v32, v32, v37, s25
	v_add3_u32 v33, v33, v36, s25
	v_and_b32_sdwa v36, v35, v231 dst_sel:DWORD dst_unused:UNUSED_PAD src0_sel:WORD_1 src1_sel:DWORD
	v_and_b32_sdwa v37, v34, v231 dst_sel:DWORD dst_unused:UNUSED_PAD src0_sel:WORD_1 src1_sel:DWORD
	v_add3_u32 v35, v35, v36, s25
	v_add3_u32 v34, v34, v37, s25
	v_and_b32_e32 v35, 0xffff0000, v35
	v_and_b32_e32 v34, 0xffff0000, v34
	v_or_b32_sdwa v33, v35, v33 dst_sel:DWORD dst_unused:UNUSED_PAD src0_sel:DWORD src1_sel:WORD_1
	v_or_b32_sdwa v32, v34, v32 dst_sel:DWORD dst_unused:UNUSED_PAD src0_sel:DWORD src1_sel:WORD_1
	global_store_dwordx2 v[64:65], v[32:33], off offset:80
	v_mov_b32_e32 v32, v40
	v_mov_b32_e32 v33, v42
	v_pk_mul_f32 v[32:33], v[32:33], v[66:67] op_sel_hi:[1,0]
	v_mov_b32_e32 v42, v41
	v_pk_mul_f32 v[34:35], v[42:43], v[66:67] op_sel_hi:[1,0]
	v_and_b32_sdwa v36, v33, v231 dst_sel:DWORD dst_unused:UNUSED_PAD src0_sel:WORD_1 src1_sel:DWORD
	v_and_b32_sdwa v37, v32, v231 dst_sel:DWORD dst_unused:UNUSED_PAD src0_sel:WORD_1 src1_sel:DWORD
	v_add3_u32 v32, v32, v37, s25
	v_add3_u32 v33, v33, v36, s25
	v_and_b32_sdwa v36, v35, v231 dst_sel:DWORD dst_unused:UNUSED_PAD src0_sel:WORD_1 src1_sel:DWORD
	v_and_b32_sdwa v37, v34, v231 dst_sel:DWORD dst_unused:UNUSED_PAD src0_sel:WORD_1 src1_sel:DWORD
	v_add3_u32 v35, v35, v36, s25
	v_add3_u32 v34, v34, v37, s25
	v_and_b32_e32 v35, 0xffff0000, v35
	v_and_b32_e32 v34, 0xffff0000, v34
	v_mfma_f32_32x32x16_bf16 v[16:31], v[92:95], v[70:73], v[16:31]
	v_or_b32_sdwa v33, v35, v33 dst_sel:DWORD dst_unused:UNUSED_PAD src0_sel:DWORD src1_sel:WORD_1
	v_or_b32_sdwa v32, v34, v32 dst_sel:DWORD dst_unused:UNUSED_PAD src0_sel:DWORD src1_sel:WORD_1
	global_store_dwordx2 v[64:65], v[32:33], off offset:96
	v_mov_b32_e32 v32, v44
	v_mov_b32_e32 v33, v46
	v_pk_mul_f32 v[32:33], v[32:33], v[66:67] op_sel_hi:[1,0]
	v_mov_b32_e32 v46, v45
	v_pk_mul_f32 v[34:35], v[46:47], v[66:67] op_sel_hi:[1,0]
	v_and_b32_sdwa v36, v33, v231 dst_sel:DWORD dst_unused:UNUSED_PAD src0_sel:WORD_1 src1_sel:DWORD
	v_and_b32_sdwa v37, v32, v231 dst_sel:DWORD dst_unused:UNUSED_PAD src0_sel:WORD_1 src1_sel:DWORD
	v_add3_u32 v32, v32, v37, s25
	v_add3_u32 v33, v33, v36, s25
	v_and_b32_sdwa v36, v35, v231 dst_sel:DWORD dst_unused:UNUSED_PAD src0_sel:WORD_1 src1_sel:DWORD
	v_and_b32_sdwa v37, v34, v231 dst_sel:DWORD dst_unused:UNUSED_PAD src0_sel:WORD_1 src1_sel:DWORD
	v_add3_u32 v35, v35, v36, s25
	v_add3_u32 v34, v34, v37, s25
	v_and_b32_e32 v35, 0xffff0000, v35
	v_and_b32_e32 v34, 0xffff0000, v34
	v_or_b32_sdwa v33, v35, v33 dst_sel:DWORD dst_unused:UNUSED_PAD src0_sel:DWORD src1_sel:WORD_1
	v_or_b32_sdwa v32, v34, v32 dst_sel:DWORD dst_unused:UNUSED_PAD src0_sel:DWORD src1_sel:WORD_1
	global_store_dwordx2 v[64:65], v[32:33], off offset:112
	v_mov_b32_e32 v32, v16
	v_mov_b32_e32 v33, v18
	v_pk_mul_f32 v[32:33], v[32:33], v[66:67] op_sel_hi:[1,0]
	v_mov_b32_e32 v18, v17
	v_pk_mul_f32 v[16:17], v[18:19], v[66:67] op_sel_hi:[1,0]
	v_and_b32_sdwa v18, v33, v231 dst_sel:DWORD dst_unused:UNUSED_PAD src0_sel:WORD_1 src1_sel:DWORD
	v_and_b32_sdwa v19, v32, v231 dst_sel:DWORD dst_unused:UNUSED_PAD src0_sel:WORD_1 src1_sel:DWORD
	v_add3_u32 v19, v32, v19, s25
	v_add3_u32 v18, v33, v18, s25
	v_and_b32_sdwa v32, v17, v231 dst_sel:DWORD dst_unused:UNUSED_PAD src0_sel:WORD_1 src1_sel:DWORD
	v_and_b32_sdwa v33, v16, v231 dst_sel:DWORD dst_unused:UNUSED_PAD src0_sel:WORD_1 src1_sel:DWORD
	v_add3_u32 v17, v17, v32, s25
	v_add3_u32 v16, v16, v33, s25
	v_and_b32_e32 v17, 0xffff0000, v17
	v_and_b32_e32 v16, 0xffff0000, v16
	v_or_b32_sdwa v17, v17, v18 dst_sel:DWORD dst_unused:UNUSED_PAD src0_sel:DWORD src1_sel:WORD_1
	v_or_b32_sdwa v16, v16, v19 dst_sel:DWORD dst_unused:UNUSED_PAD src0_sel:DWORD src1_sel:WORD_1
	global_store_dwordx2 v[64:65], v[16:17], off offset:128
	v_mov_b32_e32 v16, v20
	v_mov_b32_e32 v17, v22
	v_pk_mul_f32 v[16:17], v[16:17], v[66:67] op_sel_hi:[1,0]
	v_mov_b32_e32 v22, v21
	v_pk_mul_f32 v[18:19], v[22:23], v[66:67] op_sel_hi:[1,0]
	v_and_b32_sdwa v20, v17, v231 dst_sel:DWORD dst_unused:UNUSED_PAD src0_sel:WORD_1 src1_sel:DWORD
	v_and_b32_sdwa v21, v16, v231 dst_sel:DWORD dst_unused:UNUSED_PAD src0_sel:WORD_1 src1_sel:DWORD
	v_add3_u32 v16, v16, v21, s25
	v_add3_u32 v17, v17, v20, s25
	v_and_b32_sdwa v20, v19, v231 dst_sel:DWORD dst_unused:UNUSED_PAD src0_sel:WORD_1 src1_sel:DWORD
	v_and_b32_sdwa v21, v18, v231 dst_sel:DWORD dst_unused:UNUSED_PAD src0_sel:WORD_1 src1_sel:DWORD
	v_add3_u32 v19, v19, v20, s25
	v_add3_u32 v18, v18, v21, s25
	v_and_b32_e32 v19, 0xffff0000, v19
	v_and_b32_e32 v18, 0xffff0000, v18
	v_or_b32_sdwa v17, v19, v17 dst_sel:DWORD dst_unused:UNUSED_PAD src0_sel:DWORD src1_sel:WORD_1
	v_or_b32_sdwa v16, v18, v16 dst_sel:DWORD dst_unused:UNUSED_PAD src0_sel:DWORD src1_sel:WORD_1
	global_store_dwordx2 v[64:65], v[16:17], off offset:144
	v_mov_b32_e32 v16, v24
	v_mov_b32_e32 v17, v26
	v_pk_mul_f32 v[16:17], v[16:17], v[66:67] op_sel_hi:[1,0]
	v_mov_b32_e32 v26, v25
	v_pk_mul_f32 v[18:19], v[26:27], v[66:67] op_sel_hi:[1,0]
	v_and_b32_sdwa v20, v17, v231 dst_sel:DWORD dst_unused:UNUSED_PAD src0_sel:WORD_1 src1_sel:DWORD
	v_and_b32_sdwa v21, v16, v231 dst_sel:DWORD dst_unused:UNUSED_PAD src0_sel:WORD_1 src1_sel:DWORD
	v_add3_u32 v16, v16, v21, s25
	v_add3_u32 v17, v17, v20, s25
	v_and_b32_sdwa v20, v19, v231 dst_sel:DWORD dst_unused:UNUSED_PAD src0_sel:WORD_1 src1_sel:DWORD
	v_and_b32_sdwa v21, v18, v231 dst_sel:DWORD dst_unused:UNUSED_PAD src0_sel:WORD_1 src1_sel:DWORD
	v_add3_u32 v19, v19, v20, s25
	v_add3_u32 v18, v18, v21, s25
	v_and_b32_e32 v19, 0xffff0000, v19
	v_and_b32_e32 v18, 0xffff0000, v18
	v_mfma_f32_32x32x16_bf16 v[0:15], v[84:87], v[70:73], v[0:15]
	v_or_b32_sdwa v17, v19, v17 dst_sel:DWORD dst_unused:UNUSED_PAD src0_sel:DWORD src1_sel:WORD_1
	v_or_b32_sdwa v16, v18, v16 dst_sel:DWORD dst_unused:UNUSED_PAD src0_sel:DWORD src1_sel:WORD_1
	global_store_dwordx2 v[64:65], v[16:17], off offset:160
	v_mov_b32_e32 v16, v28
	v_mov_b32_e32 v17, v30
	v_pk_mul_f32 v[16:17], v[16:17], v[66:67] op_sel_hi:[1,0]
	v_mov_b32_e32 v30, v29
	v_pk_mul_f32 v[18:19], v[30:31], v[66:67] op_sel_hi:[1,0]
	v_and_b32_sdwa v20, v17, v231 dst_sel:DWORD dst_unused:UNUSED_PAD src0_sel:WORD_1 src1_sel:DWORD
	v_and_b32_sdwa v21, v16, v231 dst_sel:DWORD dst_unused:UNUSED_PAD src0_sel:WORD_1 src1_sel:DWORD
	v_add3_u32 v16, v16, v21, s25
	v_add3_u32 v17, v17, v20, s25
	v_and_b32_sdwa v20, v19, v231 dst_sel:DWORD dst_unused:UNUSED_PAD src0_sel:WORD_1 src1_sel:DWORD
	v_and_b32_sdwa v21, v18, v231 dst_sel:DWORD dst_unused:UNUSED_PAD src0_sel:WORD_1 src1_sel:DWORD
	v_add3_u32 v19, v19, v20, s25
	v_add3_u32 v18, v18, v21, s25
	v_and_b32_e32 v19, 0xffff0000, v19
	v_and_b32_e32 v18, 0xffff0000, v18
	v_or_b32_sdwa v17, v19, v17 dst_sel:DWORD dst_unused:UNUSED_PAD src0_sel:DWORD src1_sel:WORD_1
	v_or_b32_sdwa v16, v18, v16 dst_sel:DWORD dst_unused:UNUSED_PAD src0_sel:DWORD src1_sel:WORD_1
	global_store_dwordx2 v[64:65], v[16:17], off offset:176
	v_mov_b32_e32 v16, v0
	v_mov_b32_e32 v17, v2
	v_pk_mul_f32 v[16:17], v[16:17], v[66:67] op_sel_hi:[1,0]
	v_mov_b32_e32 v2, v1
	v_pk_mul_f32 v[0:1], v[2:3], v[66:67] op_sel_hi:[1,0]
	v_and_b32_sdwa v2, v17, v231 dst_sel:DWORD dst_unused:UNUSED_PAD src0_sel:WORD_1 src1_sel:DWORD
	v_and_b32_sdwa v3, v16, v231 dst_sel:DWORD dst_unused:UNUSED_PAD src0_sel:WORD_1 src1_sel:DWORD
	v_add3_u32 v3, v16, v3, s25
	v_add3_u32 v2, v17, v2, s25
	v_and_b32_sdwa v16, v1, v231 dst_sel:DWORD dst_unused:UNUSED_PAD src0_sel:WORD_1 src1_sel:DWORD
	v_and_b32_sdwa v17, v0, v231 dst_sel:DWORD dst_unused:UNUSED_PAD src0_sel:WORD_1 src1_sel:DWORD
	v_add3_u32 v1, v1, v16, s25
	v_add3_u32 v0, v0, v17, s25
	v_and_b32_e32 v1, 0xffff0000, v1
	v_and_b32_e32 v0, 0xffff0000, v0
	v_or_b32_sdwa v1, v1, v2 dst_sel:DWORD dst_unused:UNUSED_PAD src0_sel:DWORD src1_sel:WORD_1
	v_or_b32_sdwa v0, v0, v3 dst_sel:DWORD dst_unused:UNUSED_PAD src0_sel:DWORD src1_sel:WORD_1
	global_store_dwordx2 v[64:65], v[0:1], off offset:192
	v_mov_b32_e32 v0, v4
	v_mov_b32_e32 v1, v6
	v_pk_mul_f32 v[0:1], v[0:1], v[66:67] op_sel_hi:[1,0]
	v_mov_b32_e32 v6, v5
	v_pk_mul_f32 v[2:3], v[6:7], v[66:67] op_sel_hi:[1,0]
	v_and_b32_sdwa v4, v1, v231 dst_sel:DWORD dst_unused:UNUSED_PAD src0_sel:WORD_1 src1_sel:DWORD
	v_and_b32_sdwa v5, v0, v231 dst_sel:DWORD dst_unused:UNUSED_PAD src0_sel:WORD_1 src1_sel:DWORD
	v_add3_u32 v0, v0, v5, s25
	v_add3_u32 v1, v1, v4, s25
	v_and_b32_sdwa v4, v3, v231 dst_sel:DWORD dst_unused:UNUSED_PAD src0_sel:WORD_1 src1_sel:DWORD
	v_and_b32_sdwa v5, v2, v231 dst_sel:DWORD dst_unused:UNUSED_PAD src0_sel:WORD_1 src1_sel:DWORD
	v_add3_u32 v3, v3, v4, s25
	v_add3_u32 v2, v2, v5, s25
	v_and_b32_e32 v3, 0xffff0000, v3
	v_and_b32_e32 v2, 0xffff0000, v2
	v_or_b32_sdwa v1, v3, v1 dst_sel:DWORD dst_unused:UNUSED_PAD src0_sel:DWORD src1_sel:WORD_1
	v_or_b32_sdwa v0, v2, v0 dst_sel:DWORD dst_unused:UNUSED_PAD src0_sel:DWORD src1_sel:WORD_1
	global_store_dwordx2 v[64:65], v[0:1], off offset:208
	v_mov_b32_e32 v0, v8
	v_mov_b32_e32 v1, v10
	v_pk_mul_f32 v[0:1], v[0:1], v[66:67] op_sel_hi:[1,0]
	v_mov_b32_e32 v10, v9
	v_pk_mul_f32 v[2:3], v[10:11], v[66:67] op_sel_hi:[1,0]
	v_and_b32_sdwa v4, v1, v231 dst_sel:DWORD dst_unused:UNUSED_PAD src0_sel:WORD_1 src1_sel:DWORD
	v_and_b32_sdwa v5, v0, v231 dst_sel:DWORD dst_unused:UNUSED_PAD src0_sel:WORD_1 src1_sel:DWORD
	v_add3_u32 v0, v0, v5, s25
	v_add3_u32 v1, v1, v4, s25
	v_and_b32_sdwa v4, v3, v231 dst_sel:DWORD dst_unused:UNUSED_PAD src0_sel:WORD_1 src1_sel:DWORD
	v_and_b32_sdwa v5, v2, v231 dst_sel:DWORD dst_unused:UNUSED_PAD src0_sel:WORD_1 src1_sel:DWORD
	v_add3_u32 v3, v3, v4, s25
	v_add3_u32 v2, v2, v5, s25
	v_and_b32_e32 v3, 0xffff0000, v3
	v_and_b32_e32 v2, 0xffff0000, v2
	v_or_b32_sdwa v1, v3, v1 dst_sel:DWORD dst_unused:UNUSED_PAD src0_sel:DWORD src1_sel:WORD_1
	v_or_b32_sdwa v0, v2, v0 dst_sel:DWORD dst_unused:UNUSED_PAD src0_sel:DWORD src1_sel:WORD_1
	global_store_dwordx2 v[64:65], v[0:1], off offset:224
	v_mov_b32_e32 v0, v12
	v_mov_b32_e32 v1, v14
	v_pk_mul_f32 v[0:1], v[0:1], v[66:67] op_sel_hi:[1,0]
	v_mov_b32_e32 v14, v13
	v_pk_mul_f32 v[2:3], v[14:15], v[66:67] op_sel_hi:[1,0]
	v_and_b32_sdwa v4, v1, v231 dst_sel:DWORD dst_unused:UNUSED_PAD src0_sel:WORD_1 src1_sel:DWORD
	v_and_b32_sdwa v5, v0, v231 dst_sel:DWORD dst_unused:UNUSED_PAD src0_sel:WORD_1 src1_sel:DWORD
	v_add3_u32 v0, v0, v5, s25
	v_add3_u32 v1, v1, v4, s25
	v_and_b32_sdwa v4, v3, v231 dst_sel:DWORD dst_unused:UNUSED_PAD src0_sel:WORD_1 src1_sel:DWORD
	v_and_b32_sdwa v5, v2, v231 dst_sel:DWORD dst_unused:UNUSED_PAD src0_sel:WORD_1 src1_sel:DWORD
	v_add3_u32 v3, v3, v4, s25
	v_add3_u32 v2, v2, v5, s25
	v_and_b32_e32 v3, 0xffff0000, v3
	v_and_b32_e32 v2, 0xffff0000, v2
	v_or_b32_sdwa v1, v3, v1 dst_sel:DWORD dst_unused:UNUSED_PAD src0_sel:DWORD src1_sel:WORD_1
	v_or_b32_sdwa v0, v2, v0 dst_sel:DWORD dst_unused:UNUSED_PAD src0_sel:DWORD src1_sel:WORD_1
	global_store_dwordx2 v[64:65], v[0:1], off offset:240
	s_cbranch_scc0 .LBB0_1292
